# speedup vs baseline: 1.0103x; 1.0103x over previous
.LBB5_8:
	s_or_b64 exec, exec, s[38:39]
	v_add_u32_e32 v156, 0x8000, v142
	s_load_dwordx2 s[38:39], s[0:1], 0x78
	s_load_dwordx2 s[44:45], s[0:1], 0x68
	s_load_dwordx2 s[48:49], s[0:1], 0x28
	s_mov_b64 s[0:1], 0x80
	v_readfirstlane_b32 s61, v156
	v_add_u32_e32 v157, 0xa000, v142
	v_lshl_add_u64 v[10:11], v[10:11], 0, s[0:1]
	s_mov_b32 m0, s61
	v_readfirstlane_b32 s61, v157
	s_waitcnt vmcnt(2)
	s_barrier
	global_load_lds_dwordx4 v[10:11], off
	s_mov_b32 m0, s61
	s_add_i32 s61, 0, 0x18000
	v_add_u32_e32 v158, s61, v162
	v_lshl_add_u64 v[8:9], v[8:9], 0, s[0:1]
	v_readfirstlane_b32 s62, v158
	s_add_u32 s56, s56, 0x80080
	global_load_lds_dwordx4 v[8:9], off
	s_mov_b32 m0, s62
	v_add_u32_e32 v159, 0x2000, v158
	s_addc_u32 s57, s57, 0
	s_add_i32 s62, 0, 0x1c000
	v_lshl_add_u64 v[6:7], v[6:7], 0, s[0:1]
	v_lshl_add_u64 v[4:5], v[4:5], 0, s[0:1]
	v_readfirstlane_b32 s0, v159
	v_add_u32_e32 v160, s62, v162
	global_load_lds_dwordx4 v[6:7], off
	s_mov_b32 m0, s0
	v_readfirstlane_b32 s63, v160
	v_add_u32_e32 v161, 0x2000, v160
	global_load_lds_dwordx4 v[4:5], off
	s_mov_b32 m0, s63
	v_readfirstlane_b32 s63, v161
	global_load_lds_dwordx4 v130, s[56:57]
	s_mov_b32 m0, s63
	v_lshlrev_b32_e32 v4, 6, v0
	global_load_lds_dwordx4 v132, s[56:57]
	v_lshlrev_b32_e32 v185, 2, v0
	v_and_b32_e32 v146, 48, v0
	v_and_b32_e32 v5, 0x3c0, v4
	v_and_b32_e32 v152, 32, v185
	v_bitop3_b32 v5, v5, v152, v146 bitop3:0x36
	s_add_u32 s3, s54, s3
	v_add_u32_e32 v8, s35, v5
	s_addc_u32 s35, s55, 0
	s_add_u32 s30, s30, s3
	s_addc_u32 s31, s31, s35
	s_lshl_b32 s2, s2, 16
	v_and_b32_e32 v15, 0x3000, v4
	v_add_u16_e32 v4, v12, v13
	s_and_b32 s2, s2, 0x300000
	v_lshrrev_b16_e32 v6, 1, v4
	v_lshlrev_b32_e32 v4, 8, v0
	v_lshlrev_b32_e32 v7, 4, v164
	s_add_u32 s2, s52, s2
	v_and_b32_e32 v4, 0x18000, v4
	v_lshlrev_b32_e32 v3, 11, v3
	v_and_b32_e32 v7, 0x38000, v7
	s_addc_u32 s3, s53, 0
	s_waitcnt vmcnt(6)
	v_lshlrev_b32_e32 v14, 13, v14
	v_or3_b32 v4, v6, v4, v3
	v_or3_b32 v3, v6, v7, v3
	s_add_u32 s2, s28, s2
	v_add_u32_e32 v9, s60, v5
	v_add_u32_e32 v10, s61, v5
	v_add_u32_e32 v11, s62, v5
	v_add_u32_e32 v16, 0, v5
	v_or_b32_e32 v17, 0x800, v14
	v_or_b32_e32 v18, 0x1000, v14
	v_or_b32_e32 v19, 0x1800, v14
	v_lshlrev_b32_e32 v4, 1, v4
	v_mov_b32_e32 v5, v2
	v_lshlrev_b32_e32 v6, 1, v3
	v_mov_b32_e32 v7, v2
	s_addc_u32 s3, s29, s3
	s_mov_b64 s[0:1], 0x80080
	v_lshl_add_u64 v[134:135], s[30:31], 0, v[4:5]
	v_lshl_add_u64 v[136:137], s[30:31], 0, v[6:7]
	v_lshl_add_u64 v[138:139], s[2:3], 0, v[4:5]
	v_lshl_add_u64 v[140:141], s[2:3], 0, v[6:7]
	s_mov_b32 s35, -2
	s_mov_b64 s[2:3], 0
	v_add_u32_e32 v165, v8, v15
	v_add_u32_e32 v150, v16, v14
	v_add_u32_e32 v149, v16, v17
	v_add_u32_e32 v148, v16, v18
	v_add_u32_e32 v147, v16, v19
	v_add_u32_e32 v163, v9, v15
	s_mov_b64 s[28:29], 0x100
	s_mov_b64 s[30:31], 0x80100
	v_add_u32_e32 v133, v10, v15
	s_mov_b64 s[52:53], 0x180
	s_mov_b64 s[54:55], 0x80180
	v_add_u32_e32 v131, v11, v15
	v_mov_b32_e32 v3, v2
	v_mov_b32_e32 v4, v2
	v_mov_b32_e32 v6, v2
	v_mov_b32_e32 v8, v2
	v_mov_b32_e32 v9, v2
	v_mov_b32_e32 v10, v2
	v_mov_b32_e32 v11, v2
	v_mov_b32_e32 v12, v2
	v_mov_b32_e32 v13, v2
	v_mov_b32_e32 v14, v2
	v_mov_b32_e32 v15, v2
	v_mov_b32_e32 v16, v2
	v_mov_b32_e32 v17, v2
	v_mov_b32_e32 v18, v2
	v_mov_b32_e32 v19, v2
	v_mov_b32_e32 v20, v2
	v_mov_b32_e32 v21, v2
	v_mov_b32_e32 v22, v2
	v_mov_b32_e32 v23, v2
	v_mov_b32_e32 v24, v2
	v_mov_b32_e32 v25, v2
	v_mov_b32_e32 v26, v2
	v_mov_b32_e32 v27, v2
	v_mov_b32_e32 v28, v2
	v_mov_b32_e32 v29, v2
	v_mov_b32_e32 v30, v2
	v_mov_b32_e32 v31, v2
	v_mov_b32_e32 v32, v2
	v_mov_b32_e32 v33, v2
	v_mov_b32_e32 v34, v2
	v_mov_b32_e32 v35, v2
	v_mov_b32_e32 v36, v2
	v_mov_b32_e32 v37, v2
	v_mov_b32_e32 v38, v2
	v_mov_b32_e32 v39, v2
	v_mov_b32_e32 v40, v2
	v_mov_b32_e32 v41, v2
	v_mov_b32_e32 v42, v2
	v_mov_b32_e32 v43, v2
	v_mov_b32_e32 v44, v2
	v_mov_b32_e32 v45, v2
	v_mov_b32_e32 v46, v2
	v_mov_b32_e32 v47, v2
	v_mov_b32_e32 v48, v2
	v_mov_b32_e32 v49, v2
	v_mov_b32_e32 v50, v2
	v_mov_b32_e32 v51, v2
	v_mov_b32_e32 v52, v2
	v_mov_b32_e32 v53, v2
	v_mov_b32_e32 v54, v2
	v_mov_b32_e32 v55, v2
	v_mov_b32_e32 v56, v2
	v_mov_b32_e32 v57, v2
	v_mov_b32_e32 v58, v2
	v_mov_b32_e32 v59, v2
	v_mov_b32_e32 v60, v2
	v_mov_b32_e32 v61, v2
	v_mov_b32_e32 v62, v2
	v_mov_b32_e32 v63, v2
	v_mov_b32_e32 v64, v2
	v_mov_b32_e32 v65, v2
	v_mov_b32_e32 v66, v2
	v_mov_b32_e32 v67, v2
	v_mov_b32_e32 v68, v2
	v_mov_b32_e32 v69, v2
	v_mov_b32_e32 v70, v2
	v_mov_b32_e32 v71, v2
	v_mov_b32_e32 v72, v2
	v_mov_b32_e32 v73, v2
	v_mov_b32_e32 v74, v2
	v_mov_b32_e32 v75, v2
	v_mov_b32_e32 v76, v2
	v_mov_b32_e32 v77, v2
	v_mov_b32_e32 v78, v2
	v_mov_b32_e32 v79, v2
	v_mov_b32_e32 v80, v2
	v_mov_b32_e32 v81, v2
	v_mov_b32_e32 v82, v2
	v_mov_b32_e32 v83, v2
	v_mov_b32_e32 v84, v2
	v_mov_b32_e32 v85, v2
	v_mov_b32_e32 v86, v2
	v_mov_b32_e32 v87, v2
	v_mov_b32_e32 v88, v2
	v_mov_b32_e32 v89, v2
	v_mov_b32_e32 v90, v2
	v_mov_b32_e32 v91, v2
	v_mov_b32_e32 v92, v2
	v_mov_b32_e32 v93, v2
	v_mov_b32_e32 v94, v2
	v_mov_b32_e32 v95, v2
	v_mov_b32_e32 v96, v2
	v_mov_b32_e32 v97, v2
	v_mov_b32_e32 v98, v2
	v_mov_b32_e32 v99, v2
	v_mov_b32_e32 v100, v2
	v_mov_b32_e32 v101, v2
	v_mov_b32_e32 v102, v2
	v_mov_b32_e32 v103, v2
	v_mov_b32_e32 v104, v2
	v_mov_b32_e32 v105, v2
	v_mov_b32_e32 v106, v2
	v_mov_b32_e32 v107, v2
	v_mov_b32_e32 v108, v2
	v_mov_b32_e32 v109, v2
	v_mov_b32_e32 v110, v2
	v_mov_b32_e32 v111, v2
	v_mov_b32_e32 v112, v2
	v_mov_b32_e32 v113, v2
	v_mov_b32_e32 v114, v2
	v_mov_b32_e32 v115, v2
	v_mov_b32_e32 v116, v2
	v_mov_b32_e32 v117, v2
	v_mov_b32_e32 v118, v2
	v_mov_b32_e32 v119, v2
	v_mov_b32_e32 v120, v2
	v_mov_b32_e32 v121, v2
	v_mov_b32_e32 v122, v2
	v_mov_b32_e32 v123, v2
	v_mov_b32_e32 v124, v2
	v_mov_b32_e32 v125, v2
	v_mov_b32_e32 v126, v2
	v_mov_b32_e32 v127, v2
	v_mov_b32_e32 v128, v2
	v_mov_b32_e32 v129, v2
	v_lshrrev_b32_e32 v190, 2, v0
	v_and_b32_e32 v186, 48, v162
	v_and_b32_e32 v188, 15, v0
	v_add_u32_e32 v166, 0xc000, v142
	v_add_u32_e32 v167, 0xe000, v142
	s_barrier
	v_readfirstlane_b32 s80, v166
	v_readfirstlane_b32 s81, v167
	v_readfirstlane_b32 s82, v144
	v_readfirstlane_b32 s83, v145
	v_readfirstlane_b32 s84, v142
	v_readfirstlane_b32 s85, v143
	v_readfirstlane_b32 s86, v154
	v_readfirstlane_b32 s87, v155
	v_readfirstlane_b32 s88, v151
	v_readfirstlane_b32 s89, v153
	v_readfirstlane_b32 s90, v158
	v_readfirstlane_b32 s91, v159
	v_readfirstlane_b32 s92, v156
	v_readfirstlane_b32 s93, v157
	v_readfirstlane_b32 s94, v160
	v_readfirstlane_b32 s95, v161
.LBB5_9:
	ds_read_b128 v[168:171], v165
	ds_read_b128 v[172:175], v165 offset:1024
	ds_read_b128 v[176:179], v165 offset:2048
	ds_read_b128 v[192:195], v165 offset:3072
	v_lshl_add_u64 v[244:245], v[138:139], 0, s[2:3]
	s_mov_b32 s56, s80
	v_lshl_add_u64 v[196:197], v[244:245], 0, s[0:1]
	s_mov_b32 m0, s56
	v_lshl_add_u64 v[246:247], v[140:141], 0, s[2:3]
	s_mov_b32 s56, s81
	global_load_lds_dwordx4 v[196:197], off
	v_lshl_add_u64 v[196:197], v[246:247], 0, s[0:1]
	s_mov_b32 m0, s56
	s_nop 0
	global_load_lds_dwordx4 v[196:197], off
	ds_read_b128 v[196:199], v150
	ds_read_b128 v[200:203], v150 offset:1024
	ds_read_b128 v[204:207], v149
	ds_read_b128 v[208:211], v149 offset:1024
	ds_read_b128 v[212:215], v148
	ds_read_b128 v[216:219], v148 offset:1024
	ds_read_b128 v[220:223], v147
	ds_read_b128 v[224:227], v147 offset:1024
	s_waitcnt lgkmcnt(8)
	s_barrier
	s_waitcnt lgkmcnt(0)
	s_setprio 1
	s_waitcnt lgkmcnt(0)
	v_mfma_f32_16x16x32_f16 v[126:129], v[168:171], v[196:199], v[126:129]
	v_mfma_f32_16x16x32_f16 v[122:125], v[176:179], v[196:199], v[122:125]
	v_mfma_f32_16x16x32_f16 v[118:121], v[168:171], v[204:207], v[118:121]
	v_mfma_f32_16x16x32_f16 v[114:117], v[176:179], v[204:207], v[114:117]
	v_mfma_f32_16x16x32_f16 v[110:113], v[168:171], v[212:215], v[110:113]
	v_mfma_f32_16x16x32_f16 v[106:109], v[176:179], v[212:215], v[106:109]
	v_mfma_f32_16x16x32_f16 v[102:105], v[168:171], v[220:223], v[102:105]
	v_mfma_f32_16x16x32_f16 v[98:101], v[176:179], v[220:223], v[98:101]
	v_mfma_f32_16x16x32_f16 v[126:129], v[172:175], v[200:203], v[126:129]
	v_mfma_f32_16x16x32_f16 v[122:125], v[192:195], v[200:203], v[122:125]
	v_mfma_f32_16x16x32_f16 v[118:121], v[172:175], v[208:211], v[118:121]
	v_mfma_f32_16x16x32_f16 v[114:117], v[192:195], v[208:211], v[114:117]
	v_mfma_f32_16x16x32_f16 v[110:113], v[172:175], v[216:219], v[110:113]
	v_mfma_f32_16x16x32_f16 v[106:109], v[192:195], v[216:219], v[106:109]
	v_mfma_f32_16x16x32_f16 v[102:105], v[172:175], v[224:227], v[102:105]
	v_mfma_f32_16x16x32_f16 v[98:101], v[192:195], v[224:227], v[98:101]
	s_setprio 0
	s_barrier
	v_lshl_add_u64 v[248:249], v[134:135], 0, s[2:3]
	s_mov_b32 s56, s82
	v_lshl_add_u64 v[250:251], v[248:249], 0, s[28:29]
	s_mov_b32 m0, s56
	ds_read_b128 v[228:231], v163
	ds_read_b128 v[232:235], v163 offset:1024
	ds_read_b128 v[236:239], v163 offset:2048
	ds_read_b128 v[240:243], v163 offset:3072
	global_load_lds_dwordx4 v[250:251], off
	v_lshl_add_u64 v[250:251], v[136:137], 0, s[2:3]
	s_mov_b32 s56, s83
	v_lshl_add_u64 v[252:253], v[250:251], 0, s[28:29]
	s_mov_b32 m0, s56
	s_nop 0
	global_load_lds_dwordx4 v[252:253], off
	s_barrier
	s_waitcnt lgkmcnt(0)
	s_setprio 1
	s_waitcnt lgkmcnt(0)
	v_mfma_f32_16x16x32_f16 v[94:97], v[228:231], v[196:199], v[94:97]
	v_mfma_f32_16x16x32_f16 v[90:93], v[236:239], v[196:199], v[90:93]
	v_mfma_f32_16x16x32_f16 v[86:89], v[228:231], v[204:207], v[86:89]
	v_mfma_f32_16x16x32_f16 v[82:85], v[236:239], v[204:207], v[82:85]
	v_mfma_f32_16x16x32_f16 v[78:81], v[228:231], v[212:215], v[78:81]
	v_mfma_f32_16x16x32_f16 v[74:77], v[236:239], v[212:215], v[74:77]
	v_mfma_f32_16x16x32_f16 v[70:73], v[228:231], v[220:223], v[70:73]
	v_mfma_f32_16x16x32_f16 v[66:69], v[236:239], v[220:223], v[66:69]
	v_mfma_f32_16x16x32_f16 v[94:97], v[232:235], v[200:203], v[94:97]
	v_mfma_f32_16x16x32_f16 v[90:93], v[240:243], v[200:203], v[90:93]
	v_mfma_f32_16x16x32_f16 v[86:89], v[232:235], v[208:211], v[86:89]
	v_mfma_f32_16x16x32_f16 v[82:85], v[240:243], v[208:211], v[82:85]
	v_mfma_f32_16x16x32_f16 v[78:81], v[232:235], v[216:219], v[78:81]
	v_mfma_f32_16x16x32_f16 v[74:77], v[240:243], v[216:219], v[74:77]
	v_mfma_f32_16x16x32_f16 v[70:73], v[232:235], v[224:227], v[70:73]
	v_mfma_f32_16x16x32_f16 v[66:69], v[240:243], v[224:227], v[66:69]
	s_setprio 0
	s_mov_b32 s56, s84
	v_lshl_add_u64 v[252:253], v[244:245], 0, s[28:29]
	s_mov_b32 m0, s56
	s_mov_b32 s56, s85
	s_barrier
	ds_read_b128 v[196:199], v150 offset:16384
	ds_read_b128 v[200:203], v150 offset:17408
	ds_read_b128 v[204:207], v149 offset:16384
	ds_read_b128 v[208:211], v149 offset:17408
	ds_read_b128 v[212:215], v148 offset:16384
	ds_read_b128 v[216:219], v148 offset:17408
	ds_read_b128 v[220:223], v147 offset:16384
	ds_read_b128 v[224:227], v147 offset:17408
	global_load_lds_dwordx4 v[252:253], off
	v_lshl_add_u64 v[252:253], v[246:247], 0, s[28:29]
	s_mov_b32 m0, s56
	s_nop 0
	global_load_lds_dwordx4 v[252:253], off
	s_barrier
	s_waitcnt lgkmcnt(0)
	s_setprio 1
	s_waitcnt lgkmcnt(0)
	v_mfma_f32_16x16x32_f16 v[62:65], v[168:171], v[196:199], v[62:65]
	v_mfma_f32_16x16x32_f16 v[58:61], v[176:179], v[196:199], v[58:61]
	v_mfma_f32_16x16x32_f16 v[54:57], v[168:171], v[204:207], v[54:57]
	v_mfma_f32_16x16x32_f16 v[50:53], v[176:179], v[204:207], v[50:53]
	v_mfma_f32_16x16x32_f16 v[46:49], v[168:171], v[212:215], v[46:49]
	v_mfma_f32_16x16x32_f16 v[42:45], v[176:179], v[212:215], v[42:45]
	v_mfma_f32_16x16x32_f16 v[38:41], v[168:171], v[220:223], v[38:41]
	v_mfma_f32_16x16x32_f16 v[34:37], v[176:179], v[220:223], v[34:37]
	v_mfma_f32_16x16x32_f16 v[62:65], v[172:175], v[200:203], v[62:65]
	v_mfma_f32_16x16x32_f16 v[58:61], v[192:195], v[200:203], v[58:61]
	v_mfma_f32_16x16x32_f16 v[54:57], v[172:175], v[208:211], v[54:57]
	v_mfma_f32_16x16x32_f16 v[50:53], v[192:195], v[208:211], v[50:53]
	v_mfma_f32_16x16x32_f16 v[46:49], v[172:175], v[216:219], v[46:49]
	v_mfma_f32_16x16x32_f16 v[42:45], v[192:195], v[216:219], v[42:45]
	v_mfma_f32_16x16x32_f16 v[38:41], v[172:175], v[224:227], v[38:41]
	v_mfma_f32_16x16x32_f16 v[34:37], v[192:195], v[224:227], v[34:37]
	s_setprio 0
	s_barrier
	s_mov_b32 s56, s86
	v_lshl_add_u64 v[168:169], v[248:249], 0, s[30:31]
	s_mov_b32 m0, s56
	s_mov_b32 s56, s87
	global_load_lds_dwordx4 v[168:169], off
	v_lshl_add_u64 v[168:169], v[250:251], 0, s[30:31]
	s_mov_b32 m0, s56
	s_nop 0
	global_load_lds_dwordx4 v[168:169], off
	s_waitcnt vmcnt(6)
	s_barrier
	s_setprio 1
	v_mfma_f32_16x16x32_f16 v[30:33], v[228:231], v[196:199], v[30:33]
	v_mfma_f32_16x16x32_f16 v[26:29], v[236:239], v[196:199], v[26:29]
	v_mfma_f32_16x16x32_f16 v[22:25], v[228:231], v[204:207], v[22:25]
	v_mfma_f32_16x16x32_f16 v[18:21], v[236:239], v[204:207], v[18:21]
	v_mfma_f32_16x16x32_f16 v[14:17], v[228:231], v[212:215], v[14:17]
	v_mfma_f32_16x16x32_f16 v[10:13], v[236:239], v[212:215], v[10:13]
	v_mfma_f32_16x16x32_f16 v[6:9], v[228:231], v[220:223], v[6:9]
	v_mfma_f32_16x16x32_f16 v[2:5], v[236:239], v[220:223], v[2:5]
	v_mfma_f32_16x16x32_f16 v[30:33], v[232:235], v[200:203], v[30:33]
	v_mfma_f32_16x16x32_f16 v[26:29], v[240:243], v[200:203], v[26:29]
	v_mfma_f32_16x16x32_f16 v[22:25], v[232:235], v[208:211], v[22:25]
	v_mfma_f32_16x16x32_f16 v[18:21], v[240:243], v[208:211], v[18:21]
	v_mfma_f32_16x16x32_f16 v[14:17], v[232:235], v[216:219], v[14:17]
	v_mfma_f32_16x16x32_f16 v[10:13], v[240:243], v[216:219], v[10:13]
	v_mfma_f32_16x16x32_f16 v[6:9], v[232:235], v[224:227], v[6:9]
	v_mfma_f32_16x16x32_f16 v[2:5], v[240:243], v[224:227], v[2:5]
	s_setprio 0
	s_barrier
	ds_read_b128 v[168:171], v133
	ds_read_b128 v[172:175], v133 offset:1024
	ds_read_b128 v[176:179], v133 offset:2048
	ds_read_b128 v[192:195], v133 offset:3072
	s_mov_b32 s56, s88
	v_lshl_add_u64 v[228:229], v[244:245], 0, s[30:31]
	s_mov_b32 m0, s56
	s_mov_b32 s56, s89
	ds_read_b128 v[196:199], v150 offset:32768
	ds_read_b128 v[200:203], v150 offset:33792
	ds_read_b128 v[204:207], v149 offset:32768
	ds_read_b128 v[208:211], v149 offset:33792
	ds_read_b128 v[212:215], v148 offset:32768
	ds_read_b128 v[216:219], v148 offset:33792
	ds_read_b128 v[220:223], v147 offset:32768
	ds_read_b128 v[224:227], v147 offset:33792
	global_load_lds_dwordx4 v[228:229], off
	v_lshl_add_u64 v[228:229], v[246:247], 0, s[30:31]
	s_mov_b32 m0, s56
	s_nop 0
	global_load_lds_dwordx4 v[228:229], off
	s_waitcnt lgkmcnt(8)
	s_barrier
	s_waitcnt lgkmcnt(0)
	s_setprio 1
	s_waitcnt lgkmcnt(0)
	v_mfma_f32_16x16x32_f16 v[126:129], v[168:171], v[196:199], v[126:129]
	v_mfma_f32_16x16x32_f16 v[122:125], v[176:179], v[196:199], v[122:125]
	v_mfma_f32_16x16x32_f16 v[118:121], v[168:171], v[204:207], v[118:121]
	v_mfma_f32_16x16x32_f16 v[114:117], v[176:179], v[204:207], v[114:117]
	v_mfma_f32_16x16x32_f16 v[110:113], v[168:171], v[212:215], v[110:113]
	v_mfma_f32_16x16x32_f16 v[106:109], v[176:179], v[212:215], v[106:109]
	v_mfma_f32_16x16x32_f16 v[102:105], v[168:171], v[220:223], v[102:105]
	v_mfma_f32_16x16x32_f16 v[98:101], v[176:179], v[220:223], v[98:101]
	v_mfma_f32_16x16x32_f16 v[126:129], v[172:175], v[200:203], v[126:129]
	v_mfma_f32_16x16x32_f16 v[122:125], v[192:195], v[200:203], v[122:125]
	v_mfma_f32_16x16x32_f16 v[118:121], v[172:175], v[208:211], v[118:121]
	v_mfma_f32_16x16x32_f16 v[114:117], v[192:195], v[208:211], v[114:117]
	v_mfma_f32_16x16x32_f16 v[110:113], v[172:175], v[216:219], v[110:113]
	v_mfma_f32_16x16x32_f16 v[106:109], v[192:195], v[216:219], v[106:109]
	v_mfma_f32_16x16x32_f16 v[102:105], v[172:175], v[224:227], v[102:105]
	v_mfma_f32_16x16x32_f16 v[98:101], v[192:195], v[224:227], v[98:101]
	s_setprio 0
	s_barrier
	s_mov_b32 s56, s90
	v_lshl_add_u64 v[252:253], v[248:249], 0, s[52:53]
	s_mov_b32 m0, s56
	s_mov_b32 s56, s91
	ds_read_b128 v[228:231], v131
	ds_read_b128 v[232:235], v131 offset:1024
	ds_read_b128 v[236:239], v131 offset:2048
	ds_read_b128 v[240:243], v131 offset:3072
	global_load_lds_dwordx4 v[252:253], off
	v_lshl_add_u64 v[252:253], v[250:251], 0, s[52:53]
	s_mov_b32 m0, s56
	s_nop 0
	global_load_lds_dwordx4 v[252:253], off
	s_barrier
	s_waitcnt lgkmcnt(0)
	s_setprio 1
	s_waitcnt lgkmcnt(0)
	v_mfma_f32_16x16x32_f16 v[94:97], v[228:231], v[196:199], v[94:97]
	v_mfma_f32_16x16x32_f16 v[90:93], v[236:239], v[196:199], v[90:93]
	v_mfma_f32_16x16x32_f16 v[86:89], v[228:231], v[204:207], v[86:89]
	v_mfma_f32_16x16x32_f16 v[82:85], v[236:239], v[204:207], v[82:85]
	v_mfma_f32_16x16x32_f16 v[78:81], v[228:231], v[212:215], v[78:81]
	v_mfma_f32_16x16x32_f16 v[74:77], v[236:239], v[212:215], v[74:77]
	v_mfma_f32_16x16x32_f16 v[70:73], v[228:231], v[220:223], v[70:73]
	v_mfma_f32_16x16x32_f16 v[66:69], v[236:239], v[220:223], v[66:69]
	v_mfma_f32_16x16x32_f16 v[94:97], v[232:235], v[200:203], v[94:97]
	v_mfma_f32_16x16x32_f16 v[90:93], v[240:243], v[200:203], v[90:93]
	v_mfma_f32_16x16x32_f16 v[86:89], v[232:235], v[208:211], v[86:89]
	v_mfma_f32_16x16x32_f16 v[82:85], v[240:243], v[208:211], v[82:85]
	v_mfma_f32_16x16x32_f16 v[78:81], v[232:235], v[216:219], v[78:81]
	v_mfma_f32_16x16x32_f16 v[74:77], v[240:243], v[216:219], v[74:77]
	v_mfma_f32_16x16x32_f16 v[70:73], v[232:235], v[224:227], v[70:73]
	v_mfma_f32_16x16x32_f16 v[66:69], v[240:243], v[224:227], v[66:69]
	s_setprio 0
	s_mov_b32 s56, s92
	v_lshl_add_u64 v[244:245], v[244:245], 0, s[52:53]
	s_mov_b32 m0, s56
	s_mov_b32 s56, s93
	s_barrier
	ds_read_b128 v[196:199], v150 offset:49152
	ds_read_b128 v[200:203], v150 offset:50176
	ds_read_b128 v[204:207], v149 offset:49152
	ds_read_b128 v[208:211], v149 offset:50176
	ds_read_b128 v[212:215], v148 offset:49152
	ds_read_b128 v[216:219], v148 offset:50176
	ds_read_b128 v[220:223], v147 offset:49152
	ds_read_b128 v[224:227], v147 offset:50176
	global_load_lds_dwordx4 v[244:245], off
	v_lshl_add_u64 v[244:245], v[246:247], 0, s[52:53]
	s_mov_b32 m0, s56
	s_nop 0
	global_load_lds_dwordx4 v[244:245], off
	s_barrier
	s_waitcnt lgkmcnt(0)
	s_setprio 1
	s_waitcnt lgkmcnt(0)
	v_mfma_f32_16x16x32_f16 v[62:65], v[168:171], v[196:199], v[62:65]
	v_mfma_f32_16x16x32_f16 v[58:61], v[176:179], v[196:199], v[58:61]
	v_mfma_f32_16x16x32_f16 v[54:57], v[168:171], v[204:207], v[54:57]
	v_mfma_f32_16x16x32_f16 v[50:53], v[176:179], v[204:207], v[50:53]
	v_mfma_f32_16x16x32_f16 v[46:49], v[168:171], v[212:215], v[46:49]
	v_mfma_f32_16x16x32_f16 v[42:45], v[176:179], v[212:215], v[42:45]
	v_mfma_f32_16x16x32_f16 v[38:41], v[168:171], v[220:223], v[38:41]
	v_mfma_f32_16x16x32_f16 v[34:37], v[176:179], v[220:223], v[34:37]
	v_mfma_f32_16x16x32_f16 v[62:65], v[172:175], v[200:203], v[62:65]
	v_mfma_f32_16x16x32_f16 v[58:61], v[192:195], v[200:203], v[58:61]
	v_mfma_f32_16x16x32_f16 v[54:57], v[172:175], v[208:211], v[54:57]
	v_mfma_f32_16x16x32_f16 v[50:53], v[192:195], v[208:211], v[50:53]
	v_mfma_f32_16x16x32_f16 v[46:49], v[172:175], v[216:219], v[46:49]
	v_mfma_f32_16x16x32_f16 v[42:45], v[192:195], v[216:219], v[42:45]
	v_mfma_f32_16x16x32_f16 v[38:41], v[172:175], v[224:227], v[38:41]
	v_mfma_f32_16x16x32_f16 v[34:37], v[192:195], v[224:227], v[34:37]
	s_setprio 0
	s_barrier
	s_mov_b32 s56, s94
	v_lshl_add_u64 v[168:169], v[248:249], 0, s[54:55]
	s_mov_b32 m0, s56
	s_mov_b32 s56, s95
	global_load_lds_dwordx4 v[168:169], off
	v_lshl_add_u64 v[168:169], v[250:251], 0, s[54:55]
	s_mov_b32 m0, s56
	s_nop 0
	global_load_lds_dwordx4 v[168:169], off
	s_waitcnt vmcnt(6)
	s_barrier
	s_setprio 1
	v_mfma_f32_16x16x32_f16 v[30:33], v[228:231], v[196:199], v[30:33]
	v_mfma_f32_16x16x32_f16 v[26:29], v[236:239], v[196:199], v[26:29]
	v_mfma_f32_16x16x32_f16 v[22:25], v[228:231], v[204:207], v[22:25]
	v_mfma_f32_16x16x32_f16 v[18:21], v[236:239], v[204:207], v[18:21]
	v_mfma_f32_16x16x32_f16 v[14:17], v[228:231], v[212:215], v[14:17]
	v_mfma_f32_16x16x32_f16 v[10:13], v[236:239], v[212:215], v[10:13]
	v_mfma_f32_16x16x32_f16 v[6:9], v[228:231], v[220:223], v[6:9]
	v_mfma_f32_16x16x32_f16 v[2:5], v[236:239], v[220:223], v[2:5]
	v_mfma_f32_16x16x32_f16 v[30:33], v[232:235], v[200:203], v[30:33]
	v_mfma_f32_16x16x32_f16 v[26:29], v[240:243], v[200:203], v[26:29]
	v_mfma_f32_16x16x32_f16 v[22:25], v[232:235], v[208:211], v[22:25]
	v_mfma_f32_16x16x32_f16 v[18:21], v[240:243], v[208:211], v[18:21]
	v_mfma_f32_16x16x32_f16 v[14:17], v[232:235], v[216:219], v[14:17]
	v_mfma_f32_16x16x32_f16 v[10:13], v[240:243], v[216:219], v[10:13]
	v_mfma_f32_16x16x32_f16 v[6:9], v[232:235], v[224:227], v[6:9]
	v_mfma_f32_16x16x32_f16 v[2:5], v[240:243], v[224:227], v[2:5]
	s_setprio 0
	s_add_i32 s35, s35, 2
	s_add_u32 s2, s2, 0x100
	s_addc_u32 s3, s3, 0
	s_cmp_lt_u32 s35, 28
	s_barrier
	s_cbranch_scc1 .LBB5_9
	v_add_u32_e32 v143, 0xc000, v142
	s_add_u32 s0, s50, 0x80f80
	v_readfirstlane_b32 s2, v143
	s_addc_u32 s1, s51, 0
	s_mov_b32 m0, s2
	ds_read_b128 v[134:137], v165
	ds_read_b128 v[138:141], v165 offset:1024
	ds_read_b128 v[154:157], v165 offset:2048
	ds_read_b128 v[158:161], v165 offset:3072
	global_load_lds_dwordx4 v130, s[0:1]
	v_add_u32_e32 v130, 0xe000, v142
	s_nop 0
	v_readfirstlane_b32 s2, v130
	s_mov_b32 m0, s2
	s_nop 0
	global_load_lds_dwordx4 v132, s[0:1]
	ds_read_b128 v[142:145], v150
	ds_read_b128 v[166:169], v150 offset:1024
	ds_read_b128 v[170:173], v149
	ds_read_b128 v[174:177], v149 offset:1024
	ds_read_b128 v[192:195], v148
	ds_read_b128 v[196:199], v148 offset:1024
	ds_read_b128 v[200:203], v147
	ds_read_b128 v[204:207], v147 offset:1024
	s_barrier
	s_waitcnt lgkmcnt(0)
	s_setprio 1
	s_waitcnt lgkmcnt(0)
	v_mfma_f32_16x16x32_f16 v[126:129], v[134:137], v[142:145], v[126:129]
	v_mfma_f32_16x16x32_f16 v[122:125], v[154:157], v[142:145], v[122:125]
	v_mfma_f32_16x16x32_f16 v[118:121], v[134:137], v[170:173], v[118:121]
	v_mfma_f32_16x16x32_f16 v[114:117], v[154:157], v[170:173], v[114:117]
	v_mfma_f32_16x16x32_f16 v[110:113], v[134:137], v[192:195], v[110:113]
	v_mfma_f32_16x16x32_f16 v[106:109], v[154:157], v[192:195], v[106:109]
	v_mfma_f32_16x16x32_f16 v[102:105], v[134:137], v[200:203], v[102:105]
	v_mfma_f32_16x16x32_f16 v[98:101], v[154:157], v[200:203], v[98:101]
	v_mfma_f32_16x16x32_f16 v[126:129], v[138:141], v[166:169], v[126:129]
	v_mfma_f32_16x16x32_f16 v[122:125], v[158:161], v[166:169], v[122:125]
	v_mfma_f32_16x16x32_f16 v[118:121], v[138:141], v[174:177], v[118:121]
	v_mfma_f32_16x16x32_f16 v[114:117], v[158:161], v[174:177], v[114:117]
	v_mfma_f32_16x16x32_f16 v[110:113], v[138:141], v[196:199], v[110:113]
	v_mfma_f32_16x16x32_f16 v[106:109], v[158:161], v[196:199], v[106:109]
	v_mfma_f32_16x16x32_f16 v[102:105], v[138:141], v[204:207], v[102:105]
	v_mfma_f32_16x16x32_f16 v[98:101], v[158:161], v[204:207], v[98:101]
	s_setprio 0
	s_barrier
	ds_read_b128 v[208:211], v163
	ds_read_b128 v[212:215], v163 offset:1024
	ds_read_b128 v[216:219], v163 offset:2048
	ds_read_b128 v[220:223], v163 offset:3072
	s_barrier
	s_waitcnt lgkmcnt(0)
	s_setprio 1
	s_waitcnt lgkmcnt(0)
	v_mfma_f32_16x16x32_f16 v[86:89], v[208:211], v[170:173], v[86:89]
	v_mfma_f32_16x16x32_f16 v[82:85], v[216:219], v[170:173], v[82:85]
	v_mfma_f32_16x16x32_f16 v[78:81], v[208:211], v[192:195], v[78:81]
	v_mfma_f32_16x16x32_f16 v[74:77], v[216:219], v[192:195], v[74:77]
	v_mfma_f32_16x16x32_f16 v[70:73], v[208:211], v[200:203], v[70:73]
	v_mfma_f32_16x16x32_f16 v[66:69], v[216:219], v[200:203], v[66:69]
	v_mfma_f32_16x16x32_f16 v[94:97], v[208:211], v[142:145], v[94:97]
	v_mfma_f32_16x16x32_f16 v[90:93], v[216:219], v[142:145], v[90:93]
	v_mfma_f32_16x16x32_f16 v[86:89], v[212:215], v[174:177], v[86:89]
	v_mfma_f32_16x16x32_f16 v[82:85], v[220:223], v[174:177], v[82:85]
	v_mfma_f32_16x16x32_f16 v[78:81], v[212:215], v[196:199], v[78:81]
	v_mfma_f32_16x16x32_f16 v[74:77], v[220:223], v[196:199], v[74:77]
	v_mfma_f32_16x16x32_f16 v[70:73], v[212:215], v[204:207], v[70:73]
	v_mfma_f32_16x16x32_f16 v[66:69], v[220:223], v[204:207], v[66:69]
	v_mfma_f32_16x16x32_f16 v[224:227], v[212:215], v[166:169], v[94:97]
	v_mfma_f32_16x16x32_f16 v[166:169], v[220:223], v[166:169], v[90:93]
	s_setprio 0
	s_barrier
	s_nop 0
	ds_read_b128 v[90:93], v150 offset:16384
	ds_read_b128 v[94:97], v150 offset:17408
	ds_read_b128 v[142:145], v149 offset:16384
	ds_read_b128 v[170:173], v149 offset:17408
	ds_read_b128 v[174:177], v148 offset:16384
	ds_read_b128 v[192:195], v148 offset:17408
	ds_read_b128 v[196:199], v147 offset:16384
	ds_read_b128 v[200:203], v147 offset:17408
	s_waitcnt vmcnt(4)
	s_barrier
	s_waitcnt lgkmcnt(0)
	s_setprio 1
	s_waitcnt lgkmcnt(0)
	v_mfma_f32_16x16x32_f16 v[62:65], v[134:137], v[90:93], v[62:65]
	v_mfma_f32_16x16x32_f16 v[58:61], v[154:157], v[90:93], v[58:61]
	v_mfma_f32_16x16x32_f16 v[54:57], v[134:137], v[142:145], v[54:57]
	v_mfma_f32_16x16x32_f16 v[50:53], v[154:157], v[142:145], v[50:53]
	v_mfma_f32_16x16x32_f16 v[46:49], v[134:137], v[174:177], v[46:49]
	v_mfma_f32_16x16x32_f16 v[42:45], v[154:157], v[174:177], v[42:45]
	v_mfma_f32_16x16x32_f16 v[38:41], v[134:137], v[196:199], v[38:41]
	v_mfma_f32_16x16x32_f16 v[62:65], v[138:141], v[94:97], v[62:65]
	v_mfma_f32_16x16x32_f16 v[58:61], v[158:161], v[94:97], v[58:61]
	v_mfma_f32_16x16x32_f16 v[54:57], v[138:141], v[170:173], v[54:57]
	v_mfma_f32_16x16x32_f16 v[50:53], v[158:161], v[170:173], v[50:53]
	v_mfma_f32_16x16x32_f16 v[46:49], v[138:141], v[192:195], v[46:49]
	v_mfma_f32_16x16x32_f16 v[42:45], v[158:161], v[192:195], v[42:45]
	v_mfma_f32_16x16x32_f16 v[38:41], v[138:141], v[200:203], v[38:41]
	v_mfma_f32_16x16x32_f16 v[34:37], v[154:157], v[196:199], v[34:37]
	v_mfma_f32_16x16x32_f16 v[34:37], v[158:161], v[200:203], v[34:37]
	s_setprio 0
	s_setprio 1
	v_mfma_f32_16x16x32_f16 v[30:33], v[208:211], v[90:93], v[30:33]
	v_mfma_f32_16x16x32_f16 v[6:9], v[208:211], v[196:199], v[6:9]
	v_mfma_f32_16x16x32_f16 v[2:5], v[216:219], v[196:199], v[2:5]
	v_mfma_f32_16x16x32_f16 v[30:33], v[212:215], v[94:97], v[30:33]
	v_mfma_f32_16x16x32_f16 v[26:29], v[216:219], v[90:93], v[26:29]
	v_mfma_f32_16x16x32_f16 v[22:25], v[208:211], v[142:145], v[22:25]
	v_mfma_f32_16x16x32_f16 v[18:21], v[216:219], v[142:145], v[18:21]
	v_mfma_f32_16x16x32_f16 v[14:17], v[208:211], v[174:177], v[14:17]
	v_mfma_f32_16x16x32_f16 v[10:13], v[216:219], v[174:177], v[10:13]
	v_mfma_f32_16x16x32_f16 v[6:9], v[212:215], v[200:203], v[6:9]
	v_mfma_f32_16x16x32_f16 v[2:5], v[220:223], v[200:203], v[2:5]
	v_mfma_f32_16x16x32_f16 v[26:29], v[220:223], v[94:97], v[26:29]
	v_mfma_f32_16x16x32_f16 v[154:157], v[212:215], v[170:173], v[22:25]
	v_mfma_f32_16x16x32_f16 v[18:21], v[220:223], v[170:173], v[18:21]
	v_mfma_f32_16x16x32_f16 v[158:161], v[212:215], v[192:195], v[14:17]
	v_mfma_f32_16x16x32_f16 v[10:13], v[220:223], v[192:195], v[10:13]
	s_setprio 0
	s_barrier
	ds_read_b128 v[14:17], v133
	ds_read_b128 v[22:25], v133 offset:1024
	ds_read_b128 v[170:173], v133 offset:2048
	ds_read_b128 v[174:177], v133 offset:3072
	ds_read_b128 v[192:195], v150 offset:32768
	ds_read_b128 v[196:199], v150 offset:33792
	ds_read_b128 v[200:203], v149 offset:32768
	ds_read_b128 v[204:207], v149 offset:33792
	ds_read_b128 v[208:211], v148 offset:32768
	ds_read_b128 v[212:215], v148 offset:33792
	ds_read_b128 v[216:219], v147 offset:32768
	ds_read_b128 v[220:223], v147 offset:33792
	s_waitcnt vmcnt(2)
	s_barrier
	s_waitcnt lgkmcnt(0)
	s_setprio 1
	s_waitcnt lgkmcnt(0)
	v_mfma_f32_16x16x32_f16 v[90:93], v[14:17], v[192:195], v[126:129]
	v_mfma_f32_16x16x32_f16 v[142:145], v[22:25], v[196:199], v[90:93]
	v_mfma_f32_16x16x32_f16 v[90:93], v[170:173], v[192:195], v[122:125]
	v_mfma_f32_16x16x32_f16 v[138:141], v[174:177], v[196:199], v[90:93]
	v_mfma_f32_16x16x32_f16 v[90:93], v[14:17], v[200:203], v[118:121]
	v_mfma_f32_16x16x32_f16 v[126:129], v[22:25], v[204:207], v[90:93]
	v_mfma_f32_16x16x32_f16 v[90:93], v[170:173], v[200:203], v[114:117]
	v_mfma_f32_16x16x32_f16 v[122:125], v[174:177], v[204:207], v[90:93]
	v_mfma_f32_16x16x32_f16 v[90:93], v[14:17], v[208:211], v[110:113]
	v_mfma_f32_16x16x32_f16 v[110:113], v[22:25], v[212:215], v[90:93]
	v_mfma_f32_16x16x32_f16 v[90:93], v[170:173], v[208:211], v[106:109]
	v_mfma_f32_16x16x32_f16 v[106:109], v[174:177], v[212:215], v[90:93]
	v_mfma_f32_16x16x32_f16 v[90:93], v[14:17], v[216:219], v[102:105]
	v_mfma_f32_16x16x32_f16 v[94:97], v[22:25], v[220:223], v[90:93]
	v_mfma_f32_16x16x32_f16 v[90:93], v[170:173], v[216:219], v[98:101]
	v_mfma_f32_16x16x32_f16 v[90:93], v[174:177], v[220:223], v[90:93]
	s_setprio 0
	s_barrier
	ds_read_b128 v[228:231], v131
	ds_read_b128 v[232:235], v131 offset:1024
	ds_read_b128 v[236:239], v131 offset:2048
	ds_read_b128 v[240:243], v131 offset:3072
	s_waitcnt vmcnt(0)
	s_barrier
	s_waitcnt lgkmcnt(0)
	s_setprio 1
	s_waitcnt lgkmcnt(0)
	v_mfma_f32_16x16x32_f16 v[98:101], v[228:231], v[192:195], v[224:227]
	v_mfma_f32_16x16x32_f16 v[134:137], v[232:235], v[196:199], v[98:101]
	v_mfma_f32_16x16x32_f16 v[98:101], v[236:239], v[192:195], v[166:169]
	v_mfma_f32_16x16x32_f16 v[86:89], v[228:231], v[200:203], v[86:89]
	v_mfma_f32_16x16x32_f16 v[82:85], v[236:239], v[200:203], v[82:85]
	v_mfma_f32_16x16x32_f16 v[78:81], v[228:231], v[208:211], v[78:81]
	v_mfma_f32_16x16x32_f16 v[74:77], v[236:239], v[208:211], v[74:77]
	v_mfma_f32_16x16x32_f16 v[70:73], v[228:231], v[216:219], v[70:73]
	v_mfma_f32_16x16x32_f16 v[66:69], v[236:239], v[216:219], v[66:69]
	v_mfma_f32_16x16x32_f16 v[130:133], v[240:243], v[196:199], v[98:101]
	v_mfma_f32_16x16x32_f16 v[118:121], v[232:235], v[204:207], v[86:89]
	v_mfma_f32_16x16x32_f16 v[114:117], v[240:243], v[204:207], v[82:85]
	v_mfma_f32_16x16x32_f16 v[102:105], v[232:235], v[212:215], v[78:81]
	v_mfma_f32_16x16x32_f16 v[98:101], v[240:243], v[212:215], v[74:77]
	v_mfma_f32_16x16x32_f16 v[86:89], v[232:235], v[220:223], v[70:73]
	v_mfma_f32_16x16x32_f16 v[82:85], v[240:243], v[220:223], v[66:69]
	s_setprio 0
	s_barrier
	s_nop 0
	ds_read_b128 v[66:69], v150 offset:49152
	ds_read_b128 v[166:169], v150 offset:50176
	ds_read_b128 v[192:195], v149 offset:49152
	ds_read_b128 v[196:199], v149 offset:50176
	ds_read_b128 v[200:203], v148 offset:49152
	ds_read_b128 v[148:151], v148 offset:50176
	ds_read_b128 v[204:207], v147 offset:49152
	ds_read_b128 v[208:211], v147 offset:50176
	s_barrier
	s_waitcnt lgkmcnt(0)
	s_setprio 1
	s_waitcnt lgkmcnt(0)
	v_mfma_f32_16x16x32_f16 v[62:65], v[14:17], v[66:69], v[62:65]
	v_mfma_f32_16x16x32_f16 v[54:57], v[14:17], v[192:195], v[54:57]
	v_mfma_f32_16x16x32_f16 v[46:49], v[14:17], v[200:203], v[46:49]
	v_mfma_f32_16x16x32_f16 v[14:17], v[14:17], v[204:207], v[38:41]
	v_mfma_f32_16x16x32_f16 v[78:81], v[22:25], v[166:169], v[62:65]
	v_mfma_f32_16x16x32_f16 v[58:61], v[170:173], v[66:69], v[58:61]
	v_mfma_f32_16x16x32_f16 v[62:65], v[22:25], v[196:199], v[54:57]
	v_mfma_f32_16x16x32_f16 v[50:53], v[170:173], v[192:195], v[50:53]
	v_mfma_f32_16x16x32_f16 v[46:49], v[22:25], v[148:151], v[46:49]
	v_mfma_f32_16x16x32_f16 v[42:45], v[170:173], v[200:203], v[42:45]
	v_mfma_f32_16x16x32_f16 v[22:25], v[22:25], v[208:211], v[14:17]
	v_mfma_f32_16x16x32_f16 v[14:17], v[170:173], v[204:207], v[34:37]
	v_mfma_f32_16x16x32_f16 v[74:77], v[174:177], v[166:169], v[58:61]
	v_mfma_f32_16x16x32_f16 v[58:61], v[174:177], v[196:199], v[50:53]
	v_mfma_f32_16x16x32_f16 v[42:45], v[174:177], v[148:151], v[42:45]
	v_mfma_f32_16x16x32_f16 v[14:17], v[174:177], v[208:211], v[14:17]
	s_setprio 0
	s_setprio 1
	v_mfma_f32_16x16x32_f16 v[26:29], v[236:239], v[66:69], v[26:29]
	v_mfma_f32_16x16x32_f16 v[18:21], v[236:239], v[192:195], v[18:21]
	v_mfma_f32_16x16x32_f16 v[30:33], v[228:231], v[66:69], v[30:33]
	v_mfma_f32_16x16x32_f16 v[66:69], v[240:243], v[166:169], v[26:29]
	v_mfma_f32_16x16x32_f16 v[26:29], v[228:231], v[192:195], v[154:157]
	v_mfma_f32_16x16x32_f16 v[50:53], v[240:243], v[196:199], v[18:21]
	v_mfma_f32_16x16x32_f16 v[18:21], v[228:231], v[200:203], v[158:161]
	v_mfma_f32_16x16x32_f16 v[10:13], v[236:239], v[200:203], v[10:13]
	v_mfma_f32_16x16x32_f16 v[6:9], v[228:231], v[204:207], v[6:9]
	v_mfma_f32_16x16x32_f16 v[2:5], v[236:239], v[204:207], v[2:5]
	v_mfma_f32_16x16x32_f16 v[70:73], v[232:235], v[166:169], v[30:33]
	v_mfma_f32_16x16x32_f16 v[54:57], v[232:235], v[196:199], v[26:29]
	v_mfma_f32_16x16x32_f16 v[38:41], v[232:235], v[148:151], v[18:21]
	v_mfma_f32_16x16x32_f16 v[30:33], v[240:243], v[148:151], v[10:13]
	v_mfma_f32_16x16x32_f16 v[6:9], v[232:235], v[208:211], v[6:9]
	v_mfma_f32_16x16x32_f16 v[2:5], v[240:243], v[208:211], v[2:5]
	s_setprio 0
	s_movk_i32 s0, 0x100
	v_cmp_gt_u32_e32 vcc, s0, v0
	s_barrier
	s_and_saveexec_b64 s[0:1], vcc
	s_cbranch_execz .LBB5_12
	s_barrier
